# baseline (speedup 1.0000x reference)
.LBB3_11:
	s_xor_b64 s[2:3], s[0:1], -1
	s_cmp_lg_u32 s6, 0
	s_cbranch_scc1 .Lp3_early
	v_pk_mul_f32 v[4:5], v[98:99], v[34:35]
	v_exp_f32_e32 v6, v5
	v_exp_f32_e32 v7, v4
	v_pk_mul_f32 v[4:5], v[34:35], v[18:19]
	s_nop 0
	v_fma_f32 v5, v48, v6, v5
	v_fmac_f32_e32 v4, v7, v5
	v_pk_fma_f32 v[10:11], v[2:3], v[4:5], v[100:101]
	s_waitcnt lgkmcnt(0)
	s_barrier
	s_cmpk_gt_i32 s66, 0x2ff
	s_cbranch_scc1 .Lp3_nopf
	s_add_i32 s43, s66, 0x300
	s_ashr_i32 s60, s43, 3
	s_mul_hi_i32 s61, s60, 0x55555556
	s_lshr_b32 s62, s61, 31
	s_add_i32 s61, s61, s62
	s_mul_i32 s62, s61, 0x3fffffd
	s_add_i32 s62, s62, s60
	s_lshl_b32 s62, s62, 6
	s_lshl_b32 s63, s43, 5
	s_and_b32 s63, s63, 32
	s_or_b32 s62, s62, s63
	s_bfe_u32 s63, s43, 0x20001
	s_mul_i32 s63, s63, 0xc0
	s_add_i32 s62, s62, s63
	s_lshl_b32 s62, s62, 7
	s_lshl_b32 s63, s61, 1
	s_and_b32 s63, s63, -16
	s_add_i32 s62, s62, s63
	s_lshl_b32 s62, s62, 9
	s_lshl_b32 s63, s61, 4
	s_and_b32 s63, s63, 0x70
	s_lshl_b32 s63, s63, 2
	s_add_i32 s62, s62, s63
	s_add_u32 s44, s64, s62
	s_addc_u32 s45, s65, 0
	s_add_u32 s46, s44, 0x40000
	s_addc_u32 s47, s45, 0
	s_add_u32 s48, s46, 0x40000
	s_addc_u32 s49, s47, 0
	s_add_u32 s50, s48, 0x40000
	s_addc_u32 s51, s49, 0
	s_add_u32 s52, s50, 0x40000
	s_addc_u32 s53, s51, 0
	s_add_u32 s54, s52, 0x40000
	s_addc_u32 s55, s53, 0
	s_add_u32 s56, s54, 0x40000
	s_addc_u32 s57, s55, 0
	s_add_u32 s58, s56, 0x40000
	s_addc_u32 s59, s57, 0
	global_load_dwordx4 v[164:167], v162, s[44:45]
	global_load_dwordx4 v[164:167], v162, s[46:47]
	global_load_dwordx4 v[164:167], v162, s[48:49]
	global_load_dwordx4 v[164:167], v162, s[50:51]
	global_load_dwordx4 v[164:167], v162, s[52:53]
	global_load_dwordx4 v[164:167], v162, s[54:55]
	global_load_dwordx4 v[164:167], v162, s[56:57]
	global_load_dwordx4 v[164:167], v162, s[58:59]
.Lp3_nopf:
	v_lshl_add_u32 v8, v137, 1, v135
	ds_read_b128 v[156:159], v8
	ds_read_b128 v[6:9], v8 offset:16
	s_branch .Lp3_epi
.Lp3_early:
	v_lshl_add_u32 v8, v137, 1, v135
	ds_read_b128 v[156:159], v8
	ds_read_b128 v[6:9], v8 offset:16
	v_pk_mul_f32 v[4:5], v[98:99], v[34:35]
	v_exp_f32_e32 v14, v5
	v_exp_f32_e32 v15, v4
	v_pk_mul_f32 v[4:5], v[34:35], v[18:19]
	s_nop 0
	v_fma_f32 v5, v48, v14, v5
	v_fmac_f32_e32 v4, v15, v5
	v_pk_fma_f32 v[10:11], v[2:3], v[4:5], v[100:101]
.Lp3_epi:
	v_pk_fma_f32 v[10:11], v[94:95], v[86:87], v[10:11]
	v_pk_fma_f32 v[12:13], v[94:95], v[88:89], v[128:129]
	v_pk_fma_f32 v[2:3], v[94:95], v[82:83], v[36:37]
	v_pk_fma_f32 v[4:5], v[94:95], v[84:85], v[38:39]
	s_waitcnt lgkmcnt(1)
	v_fma_mix_f32 v10, v156, 1.0, v10 op_sel_hi:[1,0,0]
	v_fma_mix_f32 v11, v156, 1.0, v11 op_sel:[1,0,0] op_sel_hi:[1,0,0]
	v_fma_mix_f32 v12, v157, 1.0, v12 op_sel_hi:[1,0,0]
	v_fma_mix_f32 v13, v157, 1.0, v13 op_sel:[1,0,0] op_sel_hi:[1,0,0]
	ds_write_b128 v136, v[10:13]
	v_fma_mix_f32 v2, v158, 1.0, v2 op_sel_hi:[1,0,0]
	v_fma_mix_f32 v3, v158, 1.0, v3 op_sel:[1,0,0] op_sel_hi:[1,0,0]
	v_fma_mix_f32 v4, v159, 1.0, v4 op_sel_hi:[1,0,0]
	v_fma_mix_f32 v5, v159, 1.0, v5 op_sel:[1,0,0] op_sel_hi:[1,0,0]
	ds_write_b128 v136, v[2:5] offset:16
	v_pk_fma_f32 v[10:11], v[94:95], v[78:79], v[40:41]
	v_pk_fma_f32 v[12:13], v[94:95], v[80:81], v[42:43]
	v_pk_fma_f32 v[2:3], v[94:95], v[74:75], v[44:45]
	v_pk_fma_f32 v[4:5], v[94:95], v[76:77], v[46:47]
	s_waitcnt lgkmcnt(2)
	v_fma_mix_f32 v10, v6, 1.0, v10 op_sel_hi:[1,0,0]
	v_fma_mix_f32 v11, v6, 1.0, v11 op_sel:[1,0,0] op_sel_hi:[1,0,0]
	v_fma_mix_f32 v12, v7, 1.0, v12 op_sel_hi:[1,0,0]
	v_fma_mix_f32 v13, v7, 1.0, v13 op_sel:[1,0,0] op_sel_hi:[1,0,0]
	ds_write_b128 v136, v[10:13] offset:32
	v_fma_mix_f32 v2, v8, 1.0, v2 op_sel_hi:[1,0,0]
	v_fma_mix_f32 v3, v8, 1.0, v3 op_sel:[1,0,0] op_sel_hi:[1,0,0]
	v_fma_mix_f32 v4, v9, 1.0, v4 op_sel_hi:[1,0,0]
	v_fma_mix_f32 v5, v9, 1.0, v5 op_sel:[1,0,0] op_sel_hi:[1,0,0]
	ds_write_b128 v136, v[2:5] offset:48
	v_mov_b64_e32 v[92:93], v[64:65]
	v_mov_b64_e32 v[18:19], v[58:59]
	s_movk_i32 s6, 0x80
	s_mov_b64 s[0:1], 0
	s_andn2_b64 vcc, exec, s[2:3]
	v_mov_b32_e32 v138, v133
	v_mov_b32_e32 v139, v132
	v_mov_b64_e32 v[90:91], v[62:63]
	v_mov_b64_e32 v[20:21], v[60:61]
	s_cbranch_vccz .LBB3_19
